# baseline (speedup 1.0000x reference)
_Z8dog_mainPKfS0_S0_S0_S0_S0_S0_Pf:
	s_load_dwordx8 s[12:19], s[0:1], 0x0
	s_load_dwordx8 s[20:27], s[0:1], 0x20
	s_and_b32 s3, s2, 7
	s_lshl_b32 s3, s3, 5
	s_lshr_b32 s4, s2, 3
	s_add_i32 s4, s3, s4
	s_and_b32 s6, s4, 3
	s_lshr_b32 s7, s4, 2
	s_mov_b32 s5, 0
	s_lshl_b64 s[8:9], s[4:5], 18
	v_and_b32_e32 v1, 63, v0
	v_lshrrev_b32_e32 v2, 6, v0
	v_and_b32_e32 v3, 31, v0
	v_lshl_or_b32 v4, v2, 5, v3
	v_lshlrev_b32_e32 v5, 2, v4
	v_lshlrev_b32_e32 v6, 4, v1
	v_lshl_or_b32 v6, v2, 13, v6
	s_waitcnt lgkmcnt(0)
	global_load_dword v20, v5, s[18:19]
	global_load_dword v21, v5, s[20:21]
	global_load_dword v22, v5, s[22:23]
	global_load_dword v23, v5, s[24:25]
	global_load_dword v24, v5, s[14:15]
	global_load_dword v25, v5, s[16:17]
	s_add_u32 s12, s12, s8
	s_addc_u32 s13, s13, s9
	v_add_u32_e32 v31, 0x1000, v6
	global_load_dwordx4 v[128:131], v6, s[12:13] offset:0 nt
	global_load_dwordx4 v[132:135], v6, s[12:13] offset:1024 nt
	global_load_dwordx4 v[136:139], v31, s[12:13] offset:0 nt
	global_load_dwordx4 v[140:143], v31, s[12:13] offset:1024 nt
	v_add_u32_e32 v6, 0x10000, v6
	v_add_u32_e32 v31, 0x10000, v31
	global_load_dwordx4 v[144:147], v6, s[12:13] offset:0 nt
	global_load_dwordx4 v[148:151], v6, s[12:13] offset:1024 nt
	global_load_dwordx4 v[152:155], v31, s[12:13] offset:0 nt
	global_load_dwordx4 v[156:159], v31, s[12:13] offset:1024 nt
	v_bfe_u32 v7, v0, 5, 1
	v_and_b32_e32 v16, 1, v0
	v_cmp_eq_u32_e64 s[30:31], 0, v16
	v_and_b32_e32 v17, 2, v0
	v_cmp_eq_u32_e64 s[32:33], 0, v17
	v_and_b32_e32 v16, 1, v0
	v_lshrrev_b32_e32 v17, 2, v1
	v_lshlrev_b32_e32 v16, 5, v16
	v_lshl_add_u32 v16, v17, 1, v16
	v_bfe_u32 v17, v0, 1, 1
	v_lshl_add_u32 v16, v17, 7, v16
	s_movk_i32 s10, 0x110
	v_mad_u32_u24 v14, v2, s10, v16
	v_lshlrev_b32_e32 v17, 4, v7
	v_mad_u32_u24 v15, v3, s10, v17
	s_lshl_b32 s11, s6, 5
	v_lshl_add_u32 v18, v7, 2, s11
	v_cvt_f32_u32_e32 v18, v18
	v_lshlrev_b32_e32 v19, 3, v7
	v_cvt_f32_u32_e32 v19, v19
	s_waitcnt vmcnt(8)
	v_add_f32_e32 v26, v20, v21
	v_rcp_f32_e32 v27, v20
	v_rcp_f32_e32 v28, v26
	v_sub_f32_e32 v12, v19, v22
	v_sub_f32_e32 v13, v18, v23
	v_fma_f32 v29, -v20, v27, 1.0
	v_fma_f32 v30, -v26, v28, 1.0
	v_fma_f32 v27, v29, v27, v27
	v_fma_f32 v28, v30, v28, v28
	v_mul_f32_e32 v8, 0xbf38aa3b, v27
	v_mul_f32_e32 v9, 0xbf38aa3b, v28
	v_mul_f32_e32 v29, v24, v27
	v_mul_f32_e32 v30, v25, v28
	v_mul_f32_e32 v10, 0x3e22f983, v29
	v_mul_f32_e32 v11, 0x3e22f983, v30
	s_getpc_b64 s[44:45]
.Lpc_anchor:
	s_add_u32 s44, s44, _Z7dog_finPKfS0_Pf-.Lpc_anchor
	s_addc_u32 s45, s45, 0
	s_load_dwordx16 s[48:63], s[44:45], 0x0
	s_load_dwordx16 s[64:79], s[44:45], 0x40
	s_load_dwordx16 s[80:95], s[44:45], 0x80
	v_mul_f32_e32 v16, v12, v12
	v_add_f32_e32 v17, 0x3f800000, v12
	v_add_f32_e32 v18, 0x40000000, v12
	v_add_f32_e32 v19, 0x40400000, v12
	v_mul_f32_e32 v17, v17, v17
	v_mul_f32_e32 v18, v18, v18
	v_mul_f32_e32 v19, v19, v19
	v_mul_f32_e32 v20, v8, v16
	v_mul_f32_e32 v24, v9, v16
	v_mul_f32_e32 v21, v8, v17
	v_mul_f32_e32 v25, v9, v17
	v_mul_f32_e32 v22, v8, v18
	v_mul_f32_e32 v26, v9, v18
	v_mul_f32_e32 v23, v8, v19
	v_mul_f32_e32 v27, v9, v19
	v_exp_f32_e32 v20, v20
	v_exp_f32_e32 v21, v21
	v_exp_f32_e32 v22, v22
	v_exp_f32_e32 v23, v23
	v_exp_f32_e32 v24, v24
	v_exp_f32_e32 v25, v25
	v_exp_f32_e32 v26, v26
	v_exp_f32_e32 v27, v27
	v_cvt_pk_f16_f32 v32, v20, v21
	v_cvt_pk_f16_f32 v33, v22, v23
	v_cvt_pk_f16_f32 v64, v24, v25
	v_cvt_pk_f16_f32 v65, v26, v27
	v_add_f32_e32 v16, 0x40800000, v12
	v_add_f32_e32 v17, 0x40a00000, v12
	v_add_f32_e32 v18, 0x40c00000, v12
	v_add_f32_e32 v19, 0x40e00000, v12
	v_mul_f32_e32 v16, v16, v16
	v_mul_f32_e32 v17, v17, v17
	v_mul_f32_e32 v18, v18, v18
	v_mul_f32_e32 v19, v19, v19
	v_mul_f32_e32 v20, v8, v16
	v_mul_f32_e32 v24, v9, v16
	v_mul_f32_e32 v21, v8, v17
	v_mul_f32_e32 v25, v9, v17
	v_mul_f32_e32 v22, v8, v18
	v_mul_f32_e32 v26, v9, v18
	v_mul_f32_e32 v23, v8, v19
	v_mul_f32_e32 v27, v9, v19
	v_exp_f32_e32 v20, v20
	v_exp_f32_e32 v21, v21
	v_exp_f32_e32 v22, v22
	v_exp_f32_e32 v23, v23
	v_exp_f32_e32 v24, v24
	v_exp_f32_e32 v25, v25
	v_exp_f32_e32 v26, v26
	v_exp_f32_e32 v27, v27
	v_cvt_pk_f16_f32 v34, v20, v21
	v_cvt_pk_f16_f32 v35, v22, v23
	v_cvt_pk_f16_f32 v66, v24, v25
	v_cvt_pk_f16_f32 v67, v26, v27
	v_add_f32_e32 v16, 0x41800000, v12
	v_add_f32_e32 v17, 0x41880000, v12
	v_add_f32_e32 v18, 0x41900000, v12
	v_add_f32_e32 v19, 0x41980000, v12
	v_mul_f32_e32 v16, v16, v16
	v_mul_f32_e32 v17, v17, v17
	v_mul_f32_e32 v18, v18, v18
	v_mul_f32_e32 v19, v19, v19
	v_mul_f32_e32 v20, v8, v16
	v_mul_f32_e32 v24, v9, v16
	v_mul_f32_e32 v21, v8, v17
	v_mul_f32_e32 v25, v9, v17
	v_mul_f32_e32 v22, v8, v18
	v_mul_f32_e32 v26, v9, v18
	v_mul_f32_e32 v23, v8, v19
	v_mul_f32_e32 v27, v9, v19
	v_exp_f32_e32 v20, v20
	v_exp_f32_e32 v21, v21
	v_exp_f32_e32 v22, v22
	v_exp_f32_e32 v23, v23
	v_exp_f32_e32 v24, v24
	v_exp_f32_e32 v25, v25
	v_exp_f32_e32 v26, v26
	v_exp_f32_e32 v27, v27
	v_cvt_pk_f16_f32 v36, v20, v21
	v_cvt_pk_f16_f32 v37, v22, v23
	v_cvt_pk_f16_f32 v68, v24, v25
	v_cvt_pk_f16_f32 v69, v26, v27
	v_add_f32_e32 v16, 0x41a00000, v12
	v_add_f32_e32 v17, 0x41a80000, v12
	v_add_f32_e32 v18, 0x41b00000, v12
	v_add_f32_e32 v19, 0x41b80000, v12
	v_mul_f32_e32 v16, v16, v16
	v_mul_f32_e32 v17, v17, v17
	v_mul_f32_e32 v18, v18, v18
	v_mul_f32_e32 v19, v19, v19
	v_mul_f32_e32 v20, v8, v16
	v_mul_f32_e32 v24, v9, v16
	v_mul_f32_e32 v21, v8, v17
	v_mul_f32_e32 v25, v9, v17
	v_mul_f32_e32 v22, v8, v18
	v_mul_f32_e32 v26, v9, v18
	v_mul_f32_e32 v23, v8, v19
	v_mul_f32_e32 v27, v9, v19
	v_exp_f32_e32 v20, v20
	v_exp_f32_e32 v21, v21
	v_exp_f32_e32 v22, v22
	v_exp_f32_e32 v23, v23
	v_exp_f32_e32 v24, v24
	v_exp_f32_e32 v25, v25
	v_exp_f32_e32 v26, v26
	v_exp_f32_e32 v27, v27
	v_cvt_pk_f16_f32 v38, v20, v21
	v_cvt_pk_f16_f32 v39, v22, v23
	v_cvt_pk_f16_f32 v70, v24, v25
	v_cvt_pk_f16_f32 v71, v26, v27
	v_add_u32_e32 v6, 0x10000, v6
	v_add_u32_e32 v31, 0x10000, v31
	global_load_dwordx4 v[160:163], v6, s[12:13] offset:0 nt
	global_load_dwordx4 v[164:167], v6, s[12:13] offset:1024 nt
	global_load_dwordx4 v[168:171], v31, s[12:13] offset:0 nt
	global_load_dwordx4 v[172:175], v31, s[12:13] offset:1024 nt
	v_add_f32_e32 v16, 0x42000000, v12
	v_add_f32_e32 v17, 0x42040000, v12
	v_add_f32_e32 v18, 0x42080000, v12
	v_add_f32_e32 v19, 0x420c0000, v12
	v_mul_f32_e32 v16, v16, v16
	v_mul_f32_e32 v17, v17, v17
	v_mul_f32_e32 v18, v18, v18
	v_mul_f32_e32 v19, v19, v19
	v_mul_f32_e32 v20, v8, v16
	v_mul_f32_e32 v24, v9, v16
	v_mul_f32_e32 v21, v8, v17
	v_mul_f32_e32 v25, v9, v17
	v_mul_f32_e32 v22, v8, v18
	v_mul_f32_e32 v26, v9, v18
	v_mul_f32_e32 v23, v8, v19
	v_mul_f32_e32 v27, v9, v19
	v_exp_f32_e32 v20, v20
	v_exp_f32_e32 v21, v21
	v_exp_f32_e32 v22, v22
	v_exp_f32_e32 v23, v23
	v_exp_f32_e32 v24, v24
	v_exp_f32_e32 v25, v25
	v_exp_f32_e32 v26, v26
	v_exp_f32_e32 v27, v27
	v_cvt_pk_f16_f32 v40, v20, v21
	v_cvt_pk_f16_f32 v41, v22, v23
	v_cvt_pk_f16_f32 v72, v24, v25
	v_cvt_pk_f16_f32 v73, v26, v27
	v_add_f32_e32 v16, 0x42100000, v12
	v_add_f32_e32 v17, 0x42140000, v12
	v_add_f32_e32 v18, 0x42180000, v12
	v_add_f32_e32 v19, 0x421c0000, v12
	v_mul_f32_e32 v16, v16, v16
	v_mul_f32_e32 v17, v17, v17
	v_mul_f32_e32 v18, v18, v18
	v_mul_f32_e32 v19, v19, v19
	v_mul_f32_e32 v20, v8, v16
	v_mul_f32_e32 v24, v9, v16
	v_mul_f32_e32 v21, v8, v17
	v_mul_f32_e32 v25, v9, v17
	v_mul_f32_e32 v22, v8, v18
	v_mul_f32_e32 v26, v9, v18
	v_mul_f32_e32 v23, v8, v19
	v_mul_f32_e32 v27, v9, v19
	v_exp_f32_e32 v20, v20
	v_exp_f32_e32 v21, v21
	v_exp_f32_e32 v22, v22
	v_exp_f32_e32 v23, v23
	v_exp_f32_e32 v24, v24
	v_exp_f32_e32 v25, v25
	v_exp_f32_e32 v26, v26
	v_exp_f32_e32 v27, v27
	v_cvt_pk_f16_f32 v42, v20, v21
	v_cvt_pk_f16_f32 v43, v22, v23
	v_cvt_pk_f16_f32 v74, v24, v25
	v_cvt_pk_f16_f32 v75, v26, v27
	v_add_f32_e32 v16, 0x42400000, v12
	v_add_f32_e32 v17, 0x42440000, v12
	v_add_f32_e32 v18, 0x42480000, v12
	v_add_f32_e32 v19, 0x424c0000, v12
	v_mul_f32_e32 v16, v16, v16
	v_mul_f32_e32 v17, v17, v17
	v_mul_f32_e32 v18, v18, v18
	v_mul_f32_e32 v19, v19, v19
	v_mul_f32_e32 v20, v8, v16
	v_mul_f32_e32 v24, v9, v16
	v_mul_f32_e32 v21, v8, v17
	v_mul_f32_e32 v25, v9, v17
	v_mul_f32_e32 v22, v8, v18
	v_mul_f32_e32 v26, v9, v18
	v_mul_f32_e32 v23, v8, v19
	v_mul_f32_e32 v27, v9, v19
	v_exp_f32_e32 v20, v20
	v_exp_f32_e32 v21, v21
	v_exp_f32_e32 v22, v22
	v_exp_f32_e32 v23, v23
	v_exp_f32_e32 v24, v24
	v_exp_f32_e32 v25, v25
	v_exp_f32_e32 v26, v26
	v_exp_f32_e32 v27, v27
	v_cvt_pk_f16_f32 v44, v20, v21
	v_cvt_pk_f16_f32 v45, v22, v23
	v_cvt_pk_f16_f32 v76, v24, v25
	v_cvt_pk_f16_f32 v77, v26, v27
	v_add_f32_e32 v16, 0x42500000, v12
	v_add_f32_e32 v17, 0x42540000, v12
	v_add_f32_e32 v18, 0x42580000, v12
	v_add_f32_e32 v19, 0x425c0000, v12
	v_mul_f32_e32 v16, v16, v16
	v_mul_f32_e32 v17, v17, v17
	v_mul_f32_e32 v18, v18, v18
	v_mul_f32_e32 v19, v19, v19
	v_mul_f32_e32 v20, v8, v16
	v_mul_f32_e32 v24, v9, v16
	v_mul_f32_e32 v21, v8, v17
	v_mul_f32_e32 v25, v9, v17
	v_mul_f32_e32 v22, v8, v18
	v_mul_f32_e32 v26, v9, v18
	v_mul_f32_e32 v23, v8, v19
	v_mul_f32_e32 v27, v9, v19
	v_exp_f32_e32 v20, v20
	v_exp_f32_e32 v21, v21
	v_exp_f32_e32 v22, v22
	v_exp_f32_e32 v23, v23
	v_exp_f32_e32 v24, v24
	v_exp_f32_e32 v25, v25
	v_exp_f32_e32 v26, v26
	v_exp_f32_e32 v27, v27
	v_cvt_pk_f16_f32 v46, v20, v21
	v_cvt_pk_f16_f32 v47, v22, v23
	v_cvt_pk_f16_f32 v78, v24, v25
	v_cvt_pk_f16_f32 v79, v26, v27
	v_add_u32_e32 v6, 0x10000, v6
	v_add_u32_e32 v31, 0x10000, v31
	global_load_dwordx4 v[176:179], v6, s[12:13] offset:0 nt
	global_load_dwordx4 v[180:183], v6, s[12:13] offset:1024 nt
	global_load_dwordx4 v[184:187], v31, s[12:13] offset:0 nt
	global_load_dwordx4 v[188:191], v31, s[12:13] offset:1024 nt
	v_add_f32_e32 v16, 0x42800000, v12
	v_add_f32_e32 v17, 0x42820000, v12
	v_add_f32_e32 v18, 0x42840000, v12
	v_add_f32_e32 v19, 0x42860000, v12
	v_mul_f32_e32 v16, v16, v16
	v_mul_f32_e32 v17, v17, v17
	v_mul_f32_e32 v18, v18, v18
	v_mul_f32_e32 v19, v19, v19
	v_mul_f32_e32 v20, v8, v16
	v_mul_f32_e32 v24, v9, v16
	v_mul_f32_e32 v21, v8, v17
	v_mul_f32_e32 v25, v9, v17
	v_mul_f32_e32 v22, v8, v18
	v_mul_f32_e32 v26, v9, v18
	v_mul_f32_e32 v23, v8, v19
	v_mul_f32_e32 v27, v9, v19
	v_exp_f32_e32 v20, v20
	v_exp_f32_e32 v21, v21
	v_exp_f32_e32 v22, v22
	v_exp_f32_e32 v23, v23
	v_exp_f32_e32 v24, v24
	v_exp_f32_e32 v25, v25
	v_exp_f32_e32 v26, v26
	v_exp_f32_e32 v27, v27
	v_cvt_pk_f16_f32 v48, v20, v21
	v_cvt_pk_f16_f32 v49, v22, v23
	v_cvt_pk_f16_f32 v80, v24, v25
	v_cvt_pk_f16_f32 v81, v26, v27
	v_add_f32_e32 v16, 0x42880000, v12
	v_add_f32_e32 v17, 0x428a0000, v12
	v_add_f32_e32 v18, 0x428c0000, v12
	v_add_f32_e32 v19, 0x428e0000, v12
	v_mul_f32_e32 v16, v16, v16
	v_mul_f32_e32 v17, v17, v17
	v_mul_f32_e32 v18, v18, v18
	v_mul_f32_e32 v19, v19, v19
	v_mul_f32_e32 v20, v8, v16
	v_mul_f32_e32 v24, v9, v16
	v_mul_f32_e32 v21, v8, v17
	v_mul_f32_e32 v25, v9, v17
	v_mul_f32_e32 v22, v8, v18
	v_mul_f32_e32 v26, v9, v18
	v_mul_f32_e32 v23, v8, v19
	v_mul_f32_e32 v27, v9, v19
	v_exp_f32_e32 v20, v20
	v_exp_f32_e32 v21, v21
	v_exp_f32_e32 v22, v22
	v_exp_f32_e32 v23, v23
	v_exp_f32_e32 v24, v24
	v_exp_f32_e32 v25, v25
	v_exp_f32_e32 v26, v26
	v_exp_f32_e32 v27, v27
	v_cvt_pk_f16_f32 v50, v20, v21
	v_cvt_pk_f16_f32 v51, v22, v23
	v_cvt_pk_f16_f32 v82, v24, v25
	v_cvt_pk_f16_f32 v83, v26, v27
	v_add_f32_e32 v16, 0x42a00000, v12
	v_add_f32_e32 v17, 0x42a20000, v12
	v_add_f32_e32 v18, 0x42a40000, v12
	v_add_f32_e32 v19, 0x42a60000, v12
	v_mul_f32_e32 v16, v16, v16
	v_mul_f32_e32 v17, v17, v17
	v_mul_f32_e32 v18, v18, v18
	v_mul_f32_e32 v19, v19, v19
	v_mul_f32_e32 v20, v8, v16
	v_mul_f32_e32 v24, v9, v16
	v_mul_f32_e32 v21, v8, v17
	v_mul_f32_e32 v25, v9, v17
	v_mul_f32_e32 v22, v8, v18
	v_mul_f32_e32 v26, v9, v18
	v_mul_f32_e32 v23, v8, v19
	v_mul_f32_e32 v27, v9, v19
	v_exp_f32_e32 v20, v20
	v_exp_f32_e32 v21, v21
	v_exp_f32_e32 v22, v22
	v_exp_f32_e32 v23, v23
	v_exp_f32_e32 v24, v24
	v_exp_f32_e32 v25, v25
	v_exp_f32_e32 v26, v26
	v_exp_f32_e32 v27, v27
	v_cvt_pk_f16_f32 v52, v20, v21
	v_cvt_pk_f16_f32 v53, v22, v23
	v_cvt_pk_f16_f32 v84, v24, v25
	v_cvt_pk_f16_f32 v85, v26, v27
	v_add_f32_e32 v16, 0x42a80000, v12
	v_add_f32_e32 v17, 0x42aa0000, v12
	v_add_f32_e32 v18, 0x42ac0000, v12
	v_add_f32_e32 v19, 0x42ae0000, v12
	v_mul_f32_e32 v16, v16, v16
	v_mul_f32_e32 v17, v17, v17
	v_mul_f32_e32 v18, v18, v18
	v_mul_f32_e32 v19, v19, v19
	v_mul_f32_e32 v20, v8, v16
	v_mul_f32_e32 v24, v9, v16
	v_mul_f32_e32 v21, v8, v17
	v_mul_f32_e32 v25, v9, v17
	v_mul_f32_e32 v22, v8, v18
	v_mul_f32_e32 v26, v9, v18
	v_mul_f32_e32 v23, v8, v19
	v_mul_f32_e32 v27, v9, v19
	v_exp_f32_e32 v20, v20
	v_exp_f32_e32 v21, v21
	v_exp_f32_e32 v22, v22
	v_exp_f32_e32 v23, v23
	v_exp_f32_e32 v24, v24
	v_exp_f32_e32 v25, v25
	v_exp_f32_e32 v26, v26
	v_exp_f32_e32 v27, v27
	v_cvt_pk_f16_f32 v54, v20, v21
	v_cvt_pk_f16_f32 v55, v22, v23
	v_cvt_pk_f16_f32 v86, v24, v25
	v_cvt_pk_f16_f32 v87, v26, v27
	v_subrev_u32_e32 v6, 0x30000, v6
	v_subrev_u32_e32 v31, 0x30000, v31
	global_load_dwordx4 v[192:195], v6, s[12:13] offset:2048 nt
	global_load_dwordx4 v[196:199], v6, s[12:13] offset:3072 nt
	global_load_dwordx4 v[200:203], v31, s[12:13] offset:2048 nt
	global_load_dwordx4 v[204:207], v31, s[12:13] offset:3072 nt
	v_add_f32_e32 v16, 0x42c00000, v12
	v_add_f32_e32 v17, 0x42c20000, v12
	v_add_f32_e32 v18, 0x42c40000, v12
	v_add_f32_e32 v19, 0x42c60000, v12
	v_mul_f32_e32 v16, v16, v16
	v_mul_f32_e32 v17, v17, v17
	v_mul_f32_e32 v18, v18, v18
	v_mul_f32_e32 v19, v19, v19
	v_mul_f32_e32 v20, v8, v16
	v_mul_f32_e32 v24, v9, v16
	v_mul_f32_e32 v21, v8, v17
	v_mul_f32_e32 v25, v9, v17
	v_mul_f32_e32 v22, v8, v18
	v_mul_f32_e32 v26, v9, v18
	v_mul_f32_e32 v23, v8, v19
	v_mul_f32_e32 v27, v9, v19
	v_exp_f32_e32 v20, v20
	v_exp_f32_e32 v21, v21
	v_exp_f32_e32 v22, v22
	v_exp_f32_e32 v23, v23
	v_exp_f32_e32 v24, v24
	v_exp_f32_e32 v25, v25
	v_exp_f32_e32 v26, v26
	v_exp_f32_e32 v27, v27
	v_cvt_pk_f16_f32 v56, v20, v21
	v_cvt_pk_f16_f32 v57, v22, v23
	v_cvt_pk_f16_f32 v88, v24, v25
	v_cvt_pk_f16_f32 v89, v26, v27
	v_add_f32_e32 v16, 0x42c80000, v12
	v_add_f32_e32 v17, 0x42ca0000, v12
	v_add_f32_e32 v18, 0x42cc0000, v12
	v_add_f32_e32 v19, 0x42ce0000, v12
	v_mul_f32_e32 v16, v16, v16
	v_mul_f32_e32 v17, v17, v17
	v_mul_f32_e32 v18, v18, v18
	v_mul_f32_e32 v19, v19, v19
	v_mul_f32_e32 v20, v8, v16
	v_mul_f32_e32 v24, v9, v16
	v_mul_f32_e32 v21, v8, v17
	v_mul_f32_e32 v25, v9, v17
	v_mul_f32_e32 v22, v8, v18
	v_mul_f32_e32 v26, v9, v18
	v_mul_f32_e32 v23, v8, v19
	v_mul_f32_e32 v27, v9, v19
	v_exp_f32_e32 v20, v20
	v_exp_f32_e32 v21, v21
	v_exp_f32_e32 v22, v22
	v_exp_f32_e32 v23, v23
	v_exp_f32_e32 v24, v24
	v_exp_f32_e32 v25, v25
	v_exp_f32_e32 v26, v26
	v_exp_f32_e32 v27, v27
	v_cvt_pk_f16_f32 v58, v20, v21
	v_cvt_pk_f16_f32 v59, v22, v23
	v_cvt_pk_f16_f32 v90, v24, v25
	v_cvt_pk_f16_f32 v91, v26, v27
	v_add_f32_e32 v16, 0x42e00000, v12
	v_add_f32_e32 v17, 0x42e20000, v12
	v_add_f32_e32 v18, 0x42e40000, v12
	v_add_f32_e32 v19, 0x42e60000, v12
	v_mul_f32_e32 v16, v16, v16
	v_mul_f32_e32 v17, v17, v17
	v_mul_f32_e32 v18, v18, v18
	v_mul_f32_e32 v19, v19, v19
	v_mul_f32_e32 v20, v8, v16
	v_mul_f32_e32 v24, v9, v16
	v_mul_f32_e32 v21, v8, v17
	v_mul_f32_e32 v25, v9, v17
	v_mul_f32_e32 v22, v8, v18
	v_mul_f32_e32 v26, v9, v18
	v_mul_f32_e32 v23, v8, v19
	v_mul_f32_e32 v27, v9, v19
	v_exp_f32_e32 v20, v20
	v_exp_f32_e32 v21, v21
	v_exp_f32_e32 v22, v22
	v_exp_f32_e32 v23, v23
	v_exp_f32_e32 v24, v24
	v_exp_f32_e32 v25, v25
	v_exp_f32_e32 v26, v26
	v_exp_f32_e32 v27, v27
	v_cvt_pk_f16_f32 v60, v20, v21
	v_cvt_pk_f16_f32 v61, v22, v23
	v_cvt_pk_f16_f32 v92, v24, v25
	v_cvt_pk_f16_f32 v93, v26, v27
	v_add_f32_e32 v16, 0x42e80000, v12
	v_add_f32_e32 v17, 0x42ea0000, v12
	v_add_f32_e32 v18, 0x42ec0000, v12
	v_add_f32_e32 v19, 0x42ee0000, v12
	v_mul_f32_e32 v16, v16, v16
	v_mul_f32_e32 v17, v17, v17
	v_mul_f32_e32 v18, v18, v18
	v_mul_f32_e32 v19, v19, v19
	v_mul_f32_e32 v20, v8, v16
	v_mul_f32_e32 v24, v9, v16
	v_mul_f32_e32 v21, v8, v17
	v_mul_f32_e32 v25, v9, v17
	v_mul_f32_e32 v22, v8, v18
	v_mul_f32_e32 v26, v9, v18
	v_mul_f32_e32 v23, v8, v19
	v_mul_f32_e32 v27, v9, v19
	v_exp_f32_e32 v20, v20
	v_exp_f32_e32 v21, v21
	v_exp_f32_e32 v22, v22
	v_exp_f32_e32 v23, v23
	v_exp_f32_e32 v24, v24
	v_exp_f32_e32 v25, v25
	v_exp_f32_e32 v26, v26
	v_exp_f32_e32 v27, v27
	v_cvt_pk_f16_f32 v62, v20, v21
	v_cvt_pk_f16_f32 v63, v22, v23
	v_cvt_pk_f16_f32 v94, v24, v25
	v_cvt_pk_f16_f32 v95, v26, v27
	v_add_u32_e32 v6, 0x10000, v6
	v_add_u32_e32 v31, 0x10000, v31
	global_load_dwordx4 v[208:211], v6, s[12:13] offset:2048 nt
	global_load_dwordx4 v[212:215], v6, s[12:13] offset:3072 nt
	global_load_dwordx4 v[216:219], v31, s[12:13] offset:2048 nt
	global_load_dwordx4 v[220:223], v31, s[12:13] offset:3072 nt
	v_mul_f32_e32 v16, v13, v13
	v_add_f32_e32 v17, 0x3f800000, v13
	v_add_f32_e32 v18, 0x40000000, v13
	v_add_f32_e32 v19, 0x40400000, v13
	v_mul_f32_e32 v17, v17, v17
	v_mul_f32_e32 v18, v18, v18
	v_mul_f32_e32 v19, v19, v19
	v_mul_f32_e32 v20, v8, v16
	v_mul_f32_e32 v24, v9, v16
	v_mul_f32_e32 v21, v8, v17
	v_mul_f32_e32 v25, v9, v17
	v_mul_f32_e32 v22, v8, v18
	v_mul_f32_e32 v26, v9, v18
	v_mul_f32_e32 v23, v8, v19
	v_mul_f32_e32 v27, v9, v19
	v_exp_f32_e32 v20, v20
	v_exp_f32_e32 v21, v21
	v_exp_f32_e32 v22, v22
	v_exp_f32_e32 v23, v23
	v_exp_f32_e32 v24, v24
	v_exp_f32_e32 v25, v25
	v_exp_f32_e32 v26, v26
	v_exp_f32_e32 v27, v27
	v_mul_f32_e32 v96, v10, v20
	v_mul_f32_e32 v97, v10, v21
	v_mul_f32_e32 v98, v10, v22
	v_mul_f32_e32 v99, v10, v23
	v_mul_f32_e32 v112, v11, v24
	v_mul_f32_e32 v113, v11, v25
	v_mul_f32_e32 v114, v11, v26
	v_mul_f32_e32 v115, v11, v27
	v_add_f32_e32 v16, 0x41000000, v13
	v_add_f32_e32 v17, 0x41100000, v13
	v_add_f32_e32 v18, 0x41200000, v13
	v_add_f32_e32 v19, 0x41300000, v13
	v_mul_f32_e32 v16, v16, v16
	v_mul_f32_e32 v17, v17, v17
	v_mul_f32_e32 v18, v18, v18
	v_mul_f32_e32 v19, v19, v19
	v_mul_f32_e32 v20, v8, v16
	v_mul_f32_e32 v24, v9, v16
	v_mul_f32_e32 v21, v8, v17
	v_mul_f32_e32 v25, v9, v17
	v_mul_f32_e32 v22, v8, v18
	v_mul_f32_e32 v26, v9, v18
	v_mul_f32_e32 v23, v8, v19
	v_mul_f32_e32 v27, v9, v19
	v_exp_f32_e32 v20, v20
	v_exp_f32_e32 v21, v21
	v_exp_f32_e32 v22, v22
	v_exp_f32_e32 v23, v23
	v_exp_f32_e32 v24, v24
	v_exp_f32_e32 v25, v25
	v_exp_f32_e32 v26, v26
	v_exp_f32_e32 v27, v27
	v_mul_f32_e32 v100, v10, v20
	v_mul_f32_e32 v101, v10, v21
	v_mul_f32_e32 v102, v10, v22
	v_mul_f32_e32 v103, v10, v23
	v_mul_f32_e32 v116, v11, v24
	v_mul_f32_e32 v117, v11, v25
	v_mul_f32_e32 v118, v11, v26
	v_mul_f32_e32 v119, v11, v27
	v_add_u32_e32 v6, 0x10000, v6
	v_add_u32_e32 v31, 0x10000, v31
	global_load_dwordx4 v[224:227], v6, s[12:13] offset:2048 nt
	global_load_dwordx4 v[228:231], v6, s[12:13] offset:3072 nt
	global_load_dwordx4 v[232:235], v31, s[12:13] offset:2048 nt
	global_load_dwordx4 v[236:239], v31, s[12:13] offset:3072 nt
	v_add_f32_e32 v16, 0x41800000, v13
	v_add_f32_e32 v17, 0x41880000, v13
	v_add_f32_e32 v18, 0x41900000, v13
	v_add_f32_e32 v19, 0x41980000, v13
	v_mul_f32_e32 v16, v16, v16
	v_mul_f32_e32 v17, v17, v17
	v_mul_f32_e32 v18, v18, v18
	v_mul_f32_e32 v19, v19, v19
	v_mul_f32_e32 v20, v8, v16
	v_mul_f32_e32 v24, v9, v16
	v_mul_f32_e32 v21, v8, v17
	v_mul_f32_e32 v25, v9, v17
	v_mul_f32_e32 v22, v8, v18
	v_mul_f32_e32 v26, v9, v18
	v_mul_f32_e32 v23, v8, v19
	v_mul_f32_e32 v27, v9, v19
	v_exp_f32_e32 v20, v20
	v_exp_f32_e32 v21, v21
	v_exp_f32_e32 v22, v22
	v_exp_f32_e32 v23, v23
	v_exp_f32_e32 v24, v24
	v_exp_f32_e32 v25, v25
	v_exp_f32_e32 v26, v26
	v_exp_f32_e32 v27, v27
	v_mul_f32_e32 v104, v10, v20
	v_mul_f32_e32 v105, v10, v21
	v_mul_f32_e32 v106, v10, v22
	v_mul_f32_e32 v107, v10, v23
	v_mul_f32_e32 v120, v11, v24
	v_mul_f32_e32 v121, v11, v25
	v_mul_f32_e32 v122, v11, v26
	v_mul_f32_e32 v123, v11, v27
	v_add_f32_e32 v16, 0x41c00000, v13
	v_add_f32_e32 v17, 0x41c80000, v13
	v_add_f32_e32 v18, 0x41d00000, v13
	v_add_f32_e32 v19, 0x41d80000, v13
	v_mul_f32_e32 v16, v16, v16
	v_mul_f32_e32 v17, v17, v17
	v_mul_f32_e32 v18, v18, v18
	v_mul_f32_e32 v19, v19, v19
	v_mul_f32_e32 v20, v8, v16
	v_mul_f32_e32 v24, v9, v16
	v_mul_f32_e32 v21, v8, v17
	v_mul_f32_e32 v25, v9, v17
	v_mul_f32_e32 v22, v8, v18
	v_mul_f32_e32 v26, v9, v18
	v_mul_f32_e32 v23, v8, v19
	v_mul_f32_e32 v27, v9, v19
	v_exp_f32_e32 v20, v20
	v_exp_f32_e32 v21, v21
	v_exp_f32_e32 v22, v22
	v_exp_f32_e32 v23, v23
	v_exp_f32_e32 v24, v24
	v_exp_f32_e32 v25, v25
	v_exp_f32_e32 v26, v26
	v_exp_f32_e32 v27, v27
	v_mul_f32_e32 v108, v10, v20
	v_mul_f32_e32 v109, v10, v21
	v_mul_f32_e32 v110, v10, v22
	v_mul_f32_e32 v111, v10, v23
	v_mul_f32_e32 v124, v11, v24
	v_mul_f32_e32 v125, v11, v25
	v_mul_f32_e32 v126, v11, v26
	v_mul_f32_e32 v127, v11, v27
	v_add_u32_e32 v6, 0x10000, v6
	v_add_u32_e32 v31, 0x10000, v31
	global_load_dwordx4 v[240:243], v6, s[12:13] offset:2048 nt
	global_load_dwordx4 v[244:247], v6, s[12:13] offset:3072 nt
	global_load_dwordx4 v[248:251], v31, s[12:13] offset:2048 nt
	global_load_dwordx4 v[252:255], v31, s[12:13] offset:3072 nt
	s_waitcnt vmcnt(28)
	v_add_f32_e32 v128, v128, v129
	v_add_f32_e32 v130, v130, v131
	v_add_f32_e32 v132, v132, v133
	v_add_f32_e32 v134, v134, v135
	v_add_f32_e32 v136, v136, v137
	v_add_f32_e32 v138, v138, v139
	v_add_f32_e32 v140, v140, v141
	v_add_f32_e32 v142, v142, v143
	v_add_f32_e32 v128, v128, v130
	v_add_f32_e32 v132, v132, v134
	v_add_f32_e32 v136, v136, v138
	v_add_f32_e32 v140, v140, v142
	v_cndmask_b32_e64 v130, v128, v132, s[30:31]
	v_cndmask_b32_e64 v134, v136, v140, s[30:31]
	v_cndmask_b32_e64 v129, v132, v128, s[30:31]
	v_cndmask_b32_e64 v133, v140, v136, s[30:31]
	v_add_f32_dpp v129, v130, v129 quad_perm:[1,0,3,2] row_mask:0xf bank_mask:0xf bound_ctrl:1
	v_add_f32_dpp v133, v134, v133 quad_perm:[1,0,3,2] row_mask:0xf bank_mask:0xf bound_ctrl:1
	v_cndmask_b32_e64 v135, v129, v133, s[32:33]
	v_cndmask_b32_e64 v131, v133, v129, s[32:33]
	s_nop 1
	v_add_f32_dpp v131, v135, v131 quad_perm:[2,3,0,1] row_mask:0xf bank_mask:0xf bound_ctrl:1
	v_cvt_f16_f32_e32 v131, v131
	ds_write_b16 v14, v131 offset:0
	s_waitcnt vmcnt(24)
	v_add_f32_e32 v144, v144, v145
	v_add_f32_e32 v146, v146, v147
	v_add_f32_e32 v148, v148, v149
	v_add_f32_e32 v150, v150, v151
	v_add_f32_e32 v152, v152, v153
	v_add_f32_e32 v154, v154, v155
	v_add_f32_e32 v156, v156, v157
	v_add_f32_e32 v158, v158, v159
	v_add_f32_e32 v144, v144, v146
	v_add_f32_e32 v148, v148, v150
	v_add_f32_e32 v152, v152, v154
	v_add_f32_e32 v156, v156, v158
	v_cndmask_b32_e64 v146, v144, v148, s[30:31]
	v_cndmask_b32_e64 v150, v152, v156, s[30:31]
	v_cndmask_b32_e64 v145, v148, v144, s[30:31]
	v_cndmask_b32_e64 v149, v156, v152, s[30:31]
	v_add_f32_dpp v145, v146, v145 quad_perm:[1,0,3,2] row_mask:0xf bank_mask:0xf bound_ctrl:1
	v_add_f32_dpp v149, v150, v149 quad_perm:[1,0,3,2] row_mask:0xf bank_mask:0xf bound_ctrl:1
	v_cndmask_b32_e64 v151, v145, v149, s[32:33]
	v_cndmask_b32_e64 v147, v149, v145, s[32:33]
	s_nop 1
	v_add_f32_dpp v147, v151, v147 quad_perm:[2,3,0,1] row_mask:0xf bank_mask:0xf bound_ctrl:1
	v_cvt_f16_f32_e32 v147, v147
	ds_write_b16 v14, v147 offset:2176
	s_waitcnt vmcnt(20)
	v_add_f32_e32 v160, v160, v161
	v_add_f32_e32 v162, v162, v163
	v_add_f32_e32 v164, v164, v165
	v_add_f32_e32 v166, v166, v167
	v_add_f32_e32 v168, v168, v169
	v_add_f32_e32 v170, v170, v171
	v_add_f32_e32 v172, v172, v173
	v_add_f32_e32 v174, v174, v175
	v_add_f32_e32 v160, v160, v162
	v_add_f32_e32 v164, v164, v166
	v_add_f32_e32 v168, v168, v170
	v_add_f32_e32 v172, v172, v174
	v_cndmask_b32_e64 v162, v160, v164, s[30:31]
	v_cndmask_b32_e64 v166, v168, v172, s[30:31]
	v_cndmask_b32_e64 v161, v164, v160, s[30:31]
	v_cndmask_b32_e64 v165, v172, v168, s[30:31]
	v_add_f32_dpp v161, v162, v161 quad_perm:[1,0,3,2] row_mask:0xf bank_mask:0xf bound_ctrl:1
	v_add_f32_dpp v165, v166, v165 quad_perm:[1,0,3,2] row_mask:0xf bank_mask:0xf bound_ctrl:1
	v_cndmask_b32_e64 v167, v161, v165, s[32:33]
	v_cndmask_b32_e64 v163, v165, v161, s[32:33]
	s_nop 1
	v_add_f32_dpp v163, v167, v163 quad_perm:[2,3,0,1] row_mask:0xf bank_mask:0xf bound_ctrl:1
	v_cvt_f16_f32_e32 v163, v163
	ds_write_b16 v14, v163 offset:4352
	s_waitcnt vmcnt(16)
	v_add_f32_e32 v176, v176, v177
	v_add_f32_e32 v178, v178, v179
	v_add_f32_e32 v180, v180, v181
	v_add_f32_e32 v182, v182, v183
	v_add_f32_e32 v184, v184, v185
	v_add_f32_e32 v186, v186, v187
	v_add_f32_e32 v188, v188, v189
	v_add_f32_e32 v190, v190, v191
	v_add_f32_e32 v176, v176, v178
	v_add_f32_e32 v180, v180, v182
	v_add_f32_e32 v184, v184, v186
	v_add_f32_e32 v188, v188, v190
	v_cndmask_b32_e64 v178, v176, v180, s[30:31]
	v_cndmask_b32_e64 v182, v184, v188, s[30:31]
	v_cndmask_b32_e64 v177, v180, v176, s[30:31]
	v_cndmask_b32_e64 v181, v188, v184, s[30:31]
	v_add_f32_dpp v177, v178, v177 quad_perm:[1,0,3,2] row_mask:0xf bank_mask:0xf bound_ctrl:1
	v_add_f32_dpp v181, v182, v181 quad_perm:[1,0,3,2] row_mask:0xf bank_mask:0xf bound_ctrl:1
	v_cndmask_b32_e64 v183, v177, v181, s[32:33]
	v_cndmask_b32_e64 v179, v181, v177, s[32:33]
	s_nop 1
	v_add_f32_dpp v179, v183, v179 quad_perm:[2,3,0,1] row_mask:0xf bank_mask:0xf bound_ctrl:1
	v_cvt_f16_f32_e32 v179, v179
	ds_write_b16 v14, v179 offset:6528
	s_waitcnt vmcnt(12)
	v_add_f32_e32 v192, v192, v193
	v_add_f32_e32 v194, v194, v195
	v_add_f32_e32 v196, v196, v197
	v_add_f32_e32 v198, v198, v199
	v_add_f32_e32 v200, v200, v201
	v_add_f32_e32 v202, v202, v203
	v_add_f32_e32 v204, v204, v205
	v_add_f32_e32 v206, v206, v207
	v_add_f32_e32 v192, v192, v194
	v_add_f32_e32 v196, v196, v198
	v_add_f32_e32 v200, v200, v202
	v_add_f32_e32 v204, v204, v206
	v_cndmask_b32_e64 v194, v192, v196, s[30:31]
	v_cndmask_b32_e64 v198, v200, v204, s[30:31]
	v_cndmask_b32_e64 v193, v196, v192, s[30:31]
	v_cndmask_b32_e64 v197, v204, v200, s[30:31]
	v_add_f32_dpp v193, v194, v193 quad_perm:[1,0,3,2] row_mask:0xf bank_mask:0xf bound_ctrl:1
	v_add_f32_dpp v197, v198, v197 quad_perm:[1,0,3,2] row_mask:0xf bank_mask:0xf bound_ctrl:1
	v_cndmask_b32_e64 v199, v193, v197, s[32:33]
	v_cndmask_b32_e64 v195, v197, v193, s[32:33]
	s_nop 1
	v_add_f32_dpp v195, v199, v195 quad_perm:[2,3,0,1] row_mask:0xf bank_mask:0xf bound_ctrl:1
	v_cvt_f16_f32_e32 v195, v195
	ds_write_b16 v14, v195 offset:64
	s_waitcnt vmcnt(8)
	v_add_f32_e32 v208, v208, v209
	v_add_f32_e32 v210, v210, v211
	v_add_f32_e32 v212, v212, v213
	v_add_f32_e32 v214, v214, v215
	v_add_f32_e32 v216, v216, v217
	v_add_f32_e32 v218, v218, v219
	v_add_f32_e32 v220, v220, v221
	v_add_f32_e32 v222, v222, v223
	v_add_f32_e32 v208, v208, v210
	v_add_f32_e32 v212, v212, v214
	v_add_f32_e32 v216, v216, v218
	v_add_f32_e32 v220, v220, v222
	v_cndmask_b32_e64 v210, v208, v212, s[30:31]
	v_cndmask_b32_e64 v214, v216, v220, s[30:31]
	v_cndmask_b32_e64 v209, v212, v208, s[30:31]
	v_cndmask_b32_e64 v213, v220, v216, s[30:31]
	v_add_f32_dpp v209, v210, v209 quad_perm:[1,0,3,2] row_mask:0xf bank_mask:0xf bound_ctrl:1
	v_add_f32_dpp v213, v214, v213 quad_perm:[1,0,3,2] row_mask:0xf bank_mask:0xf bound_ctrl:1
	v_cndmask_b32_e64 v215, v209, v213, s[32:33]
	v_cndmask_b32_e64 v211, v213, v209, s[32:33]
	s_nop 1
	v_add_f32_dpp v211, v215, v211 quad_perm:[2,3,0,1] row_mask:0xf bank_mask:0xf bound_ctrl:1
	v_cvt_f16_f32_e32 v211, v211
	ds_write_b16 v14, v211 offset:2240
	s_waitcnt vmcnt(4)
	v_add_f32_e32 v224, v224, v225
	v_add_f32_e32 v226, v226, v227
	v_add_f32_e32 v228, v228, v229
	v_add_f32_e32 v230, v230, v231
	v_add_f32_e32 v232, v232, v233
	v_add_f32_e32 v234, v234, v235
	v_add_f32_e32 v236, v236, v237
	v_add_f32_e32 v238, v238, v239
	v_add_f32_e32 v224, v224, v226
	v_add_f32_e32 v228, v228, v230
	v_add_f32_e32 v232, v232, v234
	v_add_f32_e32 v236, v236, v238
	v_cndmask_b32_e64 v226, v224, v228, s[30:31]
	v_cndmask_b32_e64 v230, v232, v236, s[30:31]
	v_cndmask_b32_e64 v225, v228, v224, s[30:31]
	v_cndmask_b32_e64 v229, v236, v232, s[30:31]
	v_add_f32_dpp v225, v226, v225 quad_perm:[1,0,3,2] row_mask:0xf bank_mask:0xf bound_ctrl:1
	v_add_f32_dpp v229, v230, v229 quad_perm:[1,0,3,2] row_mask:0xf bank_mask:0xf bound_ctrl:1
	v_cndmask_b32_e64 v231, v225, v229, s[32:33]
	v_cndmask_b32_e64 v227, v229, v225, s[32:33]
	s_nop 1
	v_add_f32_dpp v227, v231, v227 quad_perm:[2,3,0,1] row_mask:0xf bank_mask:0xf bound_ctrl:1
	v_cvt_f16_f32_e32 v227, v227
	ds_write_b16 v14, v227 offset:4416
	s_waitcnt vmcnt(0)
	v_add_f32_e32 v240, v240, v241
	v_add_f32_e32 v242, v242, v243
	v_add_f32_e32 v244, v244, v245
	v_add_f32_e32 v246, v246, v247
	v_add_f32_e32 v248, v248, v249
	v_add_f32_e32 v250, v250, v251
	v_add_f32_e32 v252, v252, v253
	v_add_f32_e32 v254, v254, v255
	v_add_f32_e32 v240, v240, v242
	v_add_f32_e32 v244, v244, v246
	v_add_f32_e32 v248, v248, v250
	v_add_f32_e32 v252, v252, v254
	v_cndmask_b32_e64 v242, v240, v244, s[30:31]
	v_cndmask_b32_e64 v246, v248, v252, s[30:31]
	v_cndmask_b32_e64 v241, v244, v240, s[30:31]
	v_cndmask_b32_e64 v245, v252, v248, s[30:31]
	v_add_f32_dpp v241, v242, v241 quad_perm:[1,0,3,2] row_mask:0xf bank_mask:0xf bound_ctrl:1
	v_add_f32_dpp v245, v246, v245 quad_perm:[1,0,3,2] row_mask:0xf bank_mask:0xf bound_ctrl:1
	v_cndmask_b32_e64 v247, v241, v245, s[32:33]
	v_cndmask_b32_e64 v243, v245, v241, s[32:33]
	s_nop 1
	v_add_f32_dpp v243, v247, v243 quad_perm:[2,3,0,1] row_mask:0xf bank_mask:0xf bound_ctrl:1
	v_cvt_f16_f32_e32 v243, v243
	ds_write_b16 v14, v243 offset:6592
	s_waitcnt lgkmcnt(0)
	s_barrier
	ds_read_b128 v[160:163], v15 offset:0
	ds_read_b128 v[164:167], v15 offset:32
	ds_read_b128 v[168:171], v15 offset:64
	ds_read_b128 v[172:175], v15 offset:96
	ds_read_b128 v[176:179], v15 offset:128
	ds_read_b128 v[180:183], v15 offset:160
	ds_read_b128 v[184:187], v15 offset:192
	ds_read_b128 v[188:191], v15 offset:224
	s_waitcnt lgkmcnt(7)
	v_mfma_f32_32x32x16_f16 v[128:143], v[160:163], v[32:35], 0
	v_mfma_f32_32x32x16_f16 v[144:159], v[160:163], v[64:67], 0
	s_waitcnt lgkmcnt(6)
	v_mfma_f32_32x32x16_f16 v[128:143], v[164:167], v[36:39], v[128:143]
	v_mfma_f32_32x32x16_f16 v[144:159], v[164:167], v[68:71], v[144:159]
	s_waitcnt lgkmcnt(5)
	v_mfma_f32_32x32x16_f16 v[128:143], v[168:171], v[40:43], v[128:143]
	v_mfma_f32_32x32x16_f16 v[144:159], v[168:171], v[72:75], v[144:159]
	s_waitcnt lgkmcnt(4)
	v_mfma_f32_32x32x16_f16 v[128:143], v[172:175], v[44:47], v[128:143]
	v_mfma_f32_32x32x16_f16 v[144:159], v[172:175], v[76:79], v[144:159]
	s_waitcnt lgkmcnt(3)
	v_mfma_f32_32x32x16_f16 v[128:143], v[176:179], v[48:51], v[128:143]
	v_mfma_f32_32x32x16_f16 v[144:159], v[176:179], v[80:83], v[144:159]
	s_waitcnt lgkmcnt(2)
	v_mfma_f32_32x32x16_f16 v[128:143], v[180:183], v[52:55], v[128:143]
	v_mfma_f32_32x32x16_f16 v[144:159], v[180:183], v[84:87], v[144:159]
	s_waitcnt lgkmcnt(1)
	v_mfma_f32_32x32x16_f16 v[128:143], v[184:187], v[56:59], v[128:143]
	v_mfma_f32_32x32x16_f16 v[144:159], v[184:187], v[88:91], v[144:159]
	s_waitcnt lgkmcnt(0)
	v_mfma_f32_32x32x16_f16 v[128:143], v[188:191], v[60:63], v[128:143]
	v_mfma_f32_32x32x16_f16 v[144:159], v[188:191], v[92:95], v[144:159]
	s_nop 15
	s_nop 3
	v_mul_f32_e32 v16, v96, v128
	v_mul_f32_e32 v17, v97, v129
	v_mul_f32_e32 v18, v98, v130
	v_mul_f32_e32 v19, v99, v131
	v_fma_f32 v16, -v112, v144, v16
	v_fma_f32 v17, -v113, v145, v17
	v_fma_f32 v18, -v114, v146, v18
	v_fma_f32 v19, -v115, v147, v19
	v_fma_f32 v16, v100, v132, v16
	v_fma_f32 v16, -v116, v148, v16
	v_fma_f32 v17, v101, v133, v17
	v_fma_f32 v17, -v117, v149, v17
	v_fma_f32 v18, v102, v134, v18
	v_fma_f32 v18, -v118, v150, v18
	v_fma_f32 v19, v103, v135, v19
	v_fma_f32 v19, -v119, v151, v19
	v_fma_f32 v16, v104, v136, v16
	v_fma_f32 v16, -v120, v152, v16
	v_fma_f32 v17, v105, v137, v17
	v_fma_f32 v17, -v121, v153, v17
	v_fma_f32 v18, v106, v138, v18
	v_fma_f32 v18, -v122, v154, v18
	v_fma_f32 v19, v107, v139, v19
	v_fma_f32 v19, -v123, v155, v19
	v_fma_f32 v16, v108, v140, v16
	v_fma_f32 v16, -v124, v156, v16
	v_fma_f32 v17, v109, v141, v17
	v_fma_f32 v17, -v125, v157, v17
	v_fma_f32 v18, v110, v142, v18
	v_fma_f32 v18, -v126, v158, v18
	v_fma_f32 v19, v111, v143, v19
	v_fma_f32 v19, -v127, v159, v19
	v_add_f32_e32 v16, v16, v17
	v_add_f32_e32 v18, v18, v19
	v_add_f32_e32 v16, v16, v18
	v_mov_b32_e32 v17, v16
	s_lshl_b32 s6, s6, 6
	s_add_i32 s6, s6, s7
	s_lshl_b32 s6, s6, 10
	v_permlane32_swap_b32_e32 v16, v17
	v_add_u32_e32 v5, s6, v5
	v_cmp_gt_u32_e32 vcc, 32, v1
	v_add_f32_e32 v16, v16, v17
	s_and_saveexec_b64 s[2:3], vcc
	s_cbranch_execz .Ldog_main_done
	global_store_dword v5, v16, s[26:27]
